# P6 fp8 GEMM K-loop: four K-consecutive v_mfma_f32_16x16x32_fp8_fp8 per accumulator fused into one v_mfma_f32_16x16x128_f8f6f4 (same fp8 e4m3 operands, f32 accumulate, no scaling; A-fragment LDS read d
# speedup vs baseline: 1.0161x; 1.0125x over previous
; #define PG8_STAGE(bufoff, gbase, voff) do { _Pragma("unroll") for (int _i = 0; _i < 2; ++_i) \
;         __builtin_amdgcn_global_load_lds((const unsigned*)((const char*)(gbase) + (voff)[_i]), (LAS unsigned*)(lds + (bufoff) + ldsw + _i * 8192), 16, 0, 0); } while (0)
; #define PG8_LDA(dst, b, h) do { _Pragma("unroll") for (int m = 0; m < 4; ++m) _Pragma("unroll") for (int k = 0; k < 2; ++k) dst[m][k] = *(const LAS bf16x8*)(lds + PG8_SA(b, h) + aoffL + m * 2048 + k * 1024); } while (0)
; #define PG8_LDB(dst, b, h) do { _Pragma("unroll") for (int n = 0; n < 2; ++n) _Pragma("unroll") for (int k = 0; k < 2; ++k) dst[n][k] = *(const LAS bf16x8*)(lds + PG8_SB(b, h) + boffL + n * 2048 + k * 1024); } while (0)
; #define PG8_WAIT_V(n) asm volatile("s_waitcnt vmcnt(" #n ")" ::: "memory")
; #define PG8_WAIT_L(n) asm volatile("s_waitcnt lgkmcnt(" #n ")" ::: "memory")
; #define PG8_BAR __builtin_amdgcn_s_barrier()
; #define PG8_SCHED __builtin_amdgcn_sched_barrier(0)
;     ...
;             if constexpr (SP2) {
;             PG8_LDB(B0, 0, 0); PG8_LDB(B1, 0, 1); PG8_SCHED; PG8_LDA(At, 0, 0); PG8_STAGE(PG8_SA(1, 1), a1, ao1);
;             PG8_WAIT_V(8); PG8_WAIT_L(0); PG8_BAR; PG8_MMA(0, 0, At, B0); PG8_MMA(0, 1, At, B1); PG8_BAR; PG8_SCHED;
;             PG8_LDA(At, 0, 1); PG8_STAGE(PG8_SB(0, 0), b2, voffB); PG8_STAGE(PG8_SB(0, 1), b2 + hstep, voffB); PG8_STAGE(PG8_SA(0, 0), a2, x0);
;             PG8_WAIT_V(8); PG8_WAIT_L(0); PG8_BAR; PG8_MMA(1, 0, At, B0); PG8_MMA(1, 1, At, B1); PG8_BAR; PG8_SCHED;
.LBB0_1490:
	s_add_u32 s3, s8, s66
	v_add_u32_e32 v130, s87, v177
	s_addc_u32 s50, s9, s67
	ds_read_b128 v[154:157], v130
	ds_read_b128 v[158:161], v130 offset:1024
	ds_read_b128 v[146:149], v130 offset:2048
	ds_read_b128 v[150:153], v130 offset:3072
	v_add_u32_e32 v130, s88, v177
	s_add_u32 s3, s3, 0x4fc00100
	ds_read_b128 v[138:141], v130
	ds_read_b128 v[142:145], v130 offset:1024
	ds_read_b128 v[134:137], v130 offset:3072
	ds_read_b128 v[130:133], v130 offset:2048
	s_addc_u32 s52, s50, 0
	s_add_u32 s53, s92, s66
	s_addc_u32 s54, s93, s67
	s_cmpk_eq_i32 s66, 0x700
	s_cselect_b64 vcc, -1, 0
	s_and_b64 s[50:51], vcc, exec
	v_cndmask_b32_e32 v172, v183, v201, vcc
	s_cselect_b32 s71, s13, s52
	s_cselect_b32 s70, s12, s3
	v_cndmask_b32_e32 v179, v178, v202, vcc
	v_cndmask_b32_e32 v238, v176, v203, vcc
	v_cndmask_b32_e32 v181, v180, v204, vcc
	s_cselect_b32 s69, s65, s54
	s_cselect_b32 s68, s64, s53
	v_lshl_add_u64 v[230:231], v[188:189], 0, s[66:67]
	s_add_i32 m0, s74, 0xc000
	ds_read_b128 v[190:193], v200
	ds_read_b128 v[194:197], v200 offset:1024
	ds_read_b128 v[206:209], v200 offset:2048
	ds_read_b128 v[210:213], v200 offset:3072
	ds_read_b128 v[214:217], v200 offset:4096
	ds_read_b128 v[218:221], v200 offset:5120
	ds_read_b128 v[222:225], v200 offset:6144
	ds_read_b128 v[226:229], v200 offset:7168
	global_load_lds_dwordx4 v[230:231], off
	v_lshl_add_u64 v[230:231], v[186:187], 0, s[66:67]
	s_add_i32 m0, s74, 0xe000
	s_nop 0
	global_load_lds_dwordx4 v[230:231], off
	s_waitcnt vmcnt(8)
	s_waitcnt lgkmcnt(0)
	s_barrier
	s_setprio 1
	s_waitcnt lgkmcnt(0)
	v_mfma_f32_16x16x128_f8f6f4 v[126:129], v[154:161], v[190:197], v[126:129]
	v_mfma_f32_16x16x128_f8f6f4 v[122:125], v[146:153], v[190:197], v[122:125]
	v_mfma_f32_16x16x128_f8f6f4 v[118:121], v[154:161], v[206:213], v[118:121]
	v_mfma_f32_16x16x128_f8f6f4 v[106:109], v[146:153], v[206:213], v[106:109]
	v_mfma_f32_16x16x128_f8f6f4 v[94:97], v[154:161], v[214:221], v[94:97]
	v_mfma_f32_16x16x128_f8f6f4 v[90:93], v[146:153], v[214:221], v[90:93]
	v_mfma_f32_16x16x128_f8f6f4 v[78:81], v[154:161], v[222:229], v[78:81]
	v_mfma_f32_16x16x128_f8f6f4 v[74:77], v[146:153], v[222:229], v[74:77]
	s_setprio 0
	s_setprio 1
	v_mfma_f32_16x16x128_f8f6f4 v[114:117], v[138:145], v[190:197], v[114:117]
	v_mfma_f32_16x16x128_f8f6f4 v[110:113], v[130:137], v[190:197], v[110:113]
	v_mfma_f32_16x16x128_f8f6f4 v[102:105], v[138:145], v[206:213], v[102:105]
	v_mfma_f32_16x16x128_f8f6f4 v[98:101], v[130:137], v[206:213], v[98:101]
	v_mfma_f32_16x16x128_f8f6f4 v[86:89], v[138:145], v[214:221], v[86:89]
	v_mfma_f32_16x16x128_f8f6f4 v[82:85], v[130:137], v[214:221], v[82:85]
	v_mfma_f32_16x16x128_f8f6f4 v[70:73], v[138:145], v[222:229], v[70:73]
	v_mfma_f32_16x16x128_f8f6f4 v[66:69], v[130:137], v[222:229], v[66:69]
	s_setprio 0
	s_barrier
	s_add_i32 s3, s87, s59
	v_lshl_add_u64 v[190:191], s[68:69], 0, v[168:169]
	s_mov_b32 m0, s3
	ds_read_b128 v[206:209], v200 offset:16384
	ds_read_b128 v[210:213], v200 offset:17408
	ds_read_b128 v[214:217], v200 offset:18432
	ds_read_b128 v[218:221], v200 offset:19456
	ds_read_b128 v[222:225], v200 offset:20480
	ds_read_b128 v[226:229], v200 offset:21504
	ds_read_b128 v[230:233], v200 offset:22528
	ds_read_b128 v[234:237], v200 offset:23552
	global_load_lds_dwordx4 v[190:191], off
	s_add_i32 m0, s3, 0x2000
	s_add_u32 s50, s68, 0x40000
	v_lshl_add_u64 v[192:193], s[68:69], 0, v[170:171]
	s_addc_u32 s51, s69, 0
	s_add_i32 s3, s88, s59
	global_load_lds_dwordx4 v[192:193], off
	v_lshl_add_u64 v[194:195], s[50:51], 0, v[168:169]
	s_mov_b32 m0, s3
	v_mov_b32_e32 v239, v173
	global_load_lds_dwordx4 v[194:195], off
	v_lshl_add_u64 v[194:195], s[50:51], 0, v[170:171]
	s_add_i32 m0, s3, 0x2000
	v_lshl_add_u64 v[196:197], s[70:71], 0, v[172:173]
	global_load_lds_dwordx4 v[194:195], off
	s_mov_b32 m0, s74
	v_lshl_add_u64 v[194:195], s[70:71], 0, v[238:239]
	global_load_lds_dwordx4 v172, s[70:71]
	s_mov_b32 m0, s75
	s_nop 0
	global_load_lds_dwordx4 v238, s[70:71]
	s_waitcnt vmcnt(8)
	s_waitcnt lgkmcnt(0)
	s_barrier
	s_setprio 1
	s_waitcnt lgkmcnt(0)
	v_mfma_f32_16x16x128_f8f6f4 v[62:65], v[154:161], v[206:213], v[62:65]
	v_mfma_f32_16x16x128_f8f6f4 v[58:61], v[146:153], v[206:213], v[58:61]
	v_mfma_f32_16x16x128_f8f6f4 v[46:49], v[154:161], v[214:221], v[46:49]
	v_mfma_f32_16x16x128_f8f6f4 v[42:45], v[146:153], v[214:221], v[42:45]
	v_mfma_f32_16x16x128_f8f6f4 v[18:21], v[154:161], v[222:229], v[18:21]
	v_mfma_f32_16x16x128_f8f6f4 v[14:17], v[146:153], v[222:229], v[14:17]
	v_mfma_f32_16x16x128_f8f6f4 v[6:9], v[154:161], v[230:237], v[6:9]
	v_mfma_f32_16x16x128_f8f6f4 v[2:5], v[146:153], v[230:237], v[2:5]
	s_setprio 0
	s_setprio 1
	v_mfma_f32_16x16x128_f8f6f4 v[54:57], v[138:145], v[206:213], v[54:57]
	v_mfma_f32_16x16x128_f8f6f4 v[50:53], v[130:137], v[206:213], v[50:53]
	v_mfma_f32_16x16x128_f8f6f4 v[30:33], v[138:145], v[214:221], v[30:33]
	v_mfma_f32_16x16x128_f8f6f4 v[10:13], v[130:137], v[214:221], v[10:13]
	v_mfma_f32_16x16x128_f8f6f4 v[38:41], v[138:145], v[222:229], v[38:41]
	v_mfma_f32_16x16x128_f8f6f4 v[34:37], v[130:137], v[222:229], v[34:37]
	v_mfma_f32_16x16x128_f8f6f4 v[26:29], v[138:145], v[230:237], v[26:29]
	v_mfma_f32_16x16x128_f8f6f4 v[22:25], v[130:137], v[230:237], v[22:25]
	s_setprio 0
	s_barrier
; #define PG8_STAGE(bufoff, gbase, voff) do { _Pragma("unroll") for (int _i = 0; _i < 2; ++_i) \
;         __builtin_amdgcn_global_load_lds((const unsigned*)((const char*)(gbase) + (voff)[_i]), (LAS unsigned*)(lds + (bufoff) + ldsw + _i * 8192), 16, 0, 0); } while (0)
; #define PG8_LDA(dst, b, h) do { _Pragma("unroll") for (int m = 0; m < 4; ++m) _Pragma("unroll") for (int k = 0; k < 2; ++k) dst[m][k] = *(const LAS bf16x8*)(lds + PG8_SA(b, h) + aoffL + m * 2048 + k * 1024); } while (0)
; #define PG8_LDB(dst, b, h) do { _Pragma("unroll") for (int n = 0; n < 2; ++n) _Pragma("unroll") for (int k = 0; k < 2; ++k) dst[n][k] = *(const LAS bf16x8*)(lds + PG8_SB(b, h) + boffL + n * 2048 + k * 1024); } while (0)
; #define PG8_WAIT_V(n) asm volatile("s_waitcnt vmcnt(" #n ")" ::: "memory")
; #define PG8_WAIT_L(n) asm volatile("s_waitcnt lgkmcnt(" #n ")" ::: "memory")
; #define PG8_BAR __builtin_amdgcn_s_barrier()
; #define PG8_SCHED __builtin_amdgcn_sched_barrier(0)
;     ...
;             PG8_LDB(B0, 1, 0); PG8_LDB(B1, 1, 1); PG8_SCHED; PG8_LDA(At, 1, 0); PG8_STAGE(PG8_SA(0, 1), a2, x1);
;             PG8_WAIT_V(8); PG8_WAIT_L(0); PG8_BAR; PG8_MMA(0, 0, At, B0); PG8_MMA(0, 1, At, B1); PG8_BAR; PG8_SCHED;
;             PG8_LDA(At, 1, 1); PG8_STAGE(PG8_SB(1, 0), b3, voffB); PG8_STAGE(PG8_SB(1, 1), b3 + hstep, voffB); PG8_STAGE(PG8_SA(1, 0), a3, x0);
;             PG8_WAIT_V(8); PG8_WAIT_L(0); PG8_BAR; PG8_MMA(1, 0, At, B0); PG8_MMA(1, 1, At, B1); PG8_BAR; PG8_SCHED;
	s_add_i32 s3, 0, 0x18000
	v_add_u32_e32 v130, s3, v177
	s_add_i32 s52, 0, 0x1c000
	ds_read_b128 v[154:157], v130
	ds_read_b128 v[158:161], v130 offset:1024
	ds_read_b128 v[146:149], v130 offset:2048
	ds_read_b128 v[150:153], v130 offset:3072
	v_add_u32_e32 v130, s52, v177
	ds_read_b128 v[138:141], v130
	ds_read_b128 v[142:145], v130 offset:1024
	ds_read_b128 v[134:137], v130 offset:3072
	ds_read_b128 v[130:133], v130 offset:2048
	s_mov_b32 m0, s76
	ds_read_b128 v[206:209], v200 offset:32768
	ds_read_b128 v[210:213], v200 offset:33792
	ds_read_b128 v[214:217], v200 offset:34816
	ds_read_b128 v[218:221], v200 offset:35840
	ds_read_b128 v[222:225], v200 offset:36864
	ds_read_b128 v[226:229], v200 offset:37888
	ds_read_b128 v[230:233], v200 offset:38912
	ds_read_b128 v[234:237], v200 offset:39936
	global_load_lds_dwordx4 v179, s[70:71]
	s_mov_b32 m0, s77
	s_nop 0
	global_load_lds_dwordx4 v181, s[70:71]
	s_waitcnt vmcnt(8)
	s_waitcnt lgkmcnt(0)
	s_barrier
	s_setprio 1
	s_waitcnt lgkmcnt(0)
	v_mfma_f32_16x16x128_f8f6f4 v[126:129], v[154:161], v[206:213], v[126:129]
	v_mfma_f32_16x16x128_f8f6f4 v[122:125], v[146:153], v[206:213], v[122:125]
	v_mfma_f32_16x16x128_f8f6f4 v[118:121], v[154:161], v[214:221], v[118:121]
	v_mfma_f32_16x16x128_f8f6f4 v[106:109], v[146:153], v[214:221], v[106:109]
	v_mfma_f32_16x16x128_f8f6f4 v[94:97], v[154:161], v[222:229], v[94:97]
	v_mfma_f32_16x16x128_f8f6f4 v[90:93], v[146:153], v[222:229], v[90:93]
	v_mfma_f32_16x16x128_f8f6f4 v[78:81], v[154:161], v[230:237], v[78:81]
	v_mfma_f32_16x16x128_f8f6f4 v[74:77], v[146:153], v[230:237], v[74:77]
	s_setprio 0
	s_setprio 1
	v_mfma_f32_16x16x128_f8f6f4 v[114:117], v[138:145], v[206:213], v[114:117]
	v_mfma_f32_16x16x128_f8f6f4 v[110:113], v[130:137], v[206:213], v[110:113]
	v_mfma_f32_16x16x128_f8f6f4 v[102:105], v[138:145], v[214:221], v[102:105]
	v_mfma_f32_16x16x128_f8f6f4 v[98:101], v[130:137], v[214:221], v[98:101]
	v_mfma_f32_16x16x128_f8f6f4 v[86:89], v[138:145], v[222:229], v[86:89]
	v_mfma_f32_16x16x128_f8f6f4 v[82:85], v[130:137], v[222:229], v[82:85]
	v_mfma_f32_16x16x128_f8f6f4 v[70:73], v[138:145], v[230:237], v[70:73]
	v_mfma_f32_16x16x128_f8f6f4 v[66:69], v[130:137], v[230:237], v[66:69]
	s_setprio 0
	s_barrier
	s_add_i32 s3, s3, s59
	v_lshl_add_u64 v[190:191], v[190:191], 0, s[20:21]
	s_mov_b32 m0, s3
	ds_read_b128 v[206:209], v200 offset:49152
	ds_read_b128 v[210:213], v200 offset:50176
	ds_read_b128 v[214:217], v200 offset:51200
	ds_read_b128 v[218:221], v200 offset:52224
	ds_read_b128 v[222:225], v200 offset:53248
	ds_read_b128 v[226:229], v200 offset:54272
	ds_read_b128 v[230:233], v200 offset:55296
	ds_read_b128 v[234:237], v200 offset:56320
	global_load_lds_dwordx4 v[190:191], off
	s_add_i32 m0, s3, 0x2000
	s_add_u32 s50, s68, 0x40080
	v_lshl_add_u64 v[190:191], v[192:193], 0, s[20:21]
	s_addc_u32 s51, s69, 0
	s_add_i32 s3, s52, s59
	global_load_lds_dwordx4 v[190:191], off
	v_lshl_add_u64 v[190:191], s[50:51], 0, v[168:169]
	s_mov_b32 m0, s3
	s_nop 0
	global_load_lds_dwordx4 v[190:191], off
	v_lshl_add_u64 v[190:191], s[50:51], 0, v[170:171]
	s_add_i32 m0, s3, 0x2000
	s_nop 0
	global_load_lds_dwordx4 v[190:191], off
	v_lshl_add_u64 v[190:191], v[196:197], 0, s[20:21]
	s_mov_b32 m0, s79
	s_nop 0
	global_load_lds_dwordx4 v[190:191], off
	v_lshl_add_u64 v[190:191], v[194:195], 0, s[20:21]
	s_mov_b32 m0, s83
	s_nop 0
	global_load_lds_dwordx4 v[190:191], off
	s_waitcnt vmcnt(8)
	s_waitcnt lgkmcnt(0)
	s_barrier
	s_setprio 1
	s_waitcnt lgkmcnt(0)
	v_mfma_f32_16x16x128_f8f6f4 v[62:65], v[154:161], v[206:213], v[62:65]
	v_mfma_f32_16x16x128_f8f6f4 v[58:61], v[146:153], v[206:213], v[58:61]
	v_mfma_f32_16x16x128_f8f6f4 v[46:49], v[154:161], v[214:221], v[46:49]
	v_mfma_f32_16x16x128_f8f6f4 v[42:45], v[146:153], v[214:221], v[42:45]
	v_mfma_f32_16x16x128_f8f6f4 v[18:21], v[154:161], v[222:229], v[18:21]
	v_mfma_f32_16x16x128_f8f6f4 v[14:17], v[146:153], v[222:229], v[14:17]
	v_mfma_f32_16x16x128_f8f6f4 v[6:9], v[154:161], v[230:237], v[6:9]
	v_mfma_f32_16x16x128_f8f6f4 v[2:5], v[146:153], v[230:237], v[2:5]
	s_setprio 0
	s_setprio 1
	v_mfma_f32_16x16x128_f8f6f4 v[54:57], v[138:145], v[206:213], v[54:57]
	v_mfma_f32_16x16x128_f8f6f4 v[50:53], v[130:137], v[206:213], v[50:53]
	v_mfma_f32_16x16x128_f8f6f4 v[30:33], v[138:145], v[214:221], v[30:33]
	v_mfma_f32_16x16x128_f8f6f4 v[10:13], v[130:137], v[214:221], v[10:13]
	v_mfma_f32_16x16x128_f8f6f4 v[38:41], v[138:145], v[222:229], v[38:41]
	v_mfma_f32_16x16x128_f8f6f4 v[34:37], v[130:137], v[222:229], v[34:37]
	v_mfma_f32_16x16x128_f8f6f4 v[26:29], v[138:145], v[230:237], v[26:29]
	v_mfma_f32_16x16x128_f8f6f4 v[22:25], v[130:137], v[230:237], v[22:25]
	s_setprio 0
	s_barrier
	s_add_i32 s94, s94, 2
	s_add_u32 s66, s66, 0x100
	s_addc_u32 s67, s67, 0
	s_cmp_gt_u32 s94, 13
	s_cbranch_scc1 .LBB0_1493
